# 2-deep K/V prefetch in mixer-B key loops (unrolled x2, second staging register set v208-231), on top of softmax VALU diet
# baseline (speedup 1.0000x reference)
.LBB0_746:
	s_andn2_b64 vcc, exec, s[0:1]
	s_cbranch_vccnz .LBB0_434
	s_cmpk_gt_i32 s68, 0xfff
	s_mov_b64 s[0:1], -1
	s_cbranch_scc0 .LBB0_804
	s_add_i32 s0, s68, 0xfffff000
	s_lshr_b32 s80, s0, 10
	s_bfe_u32 s0, s68, 0x50003
	s_and_b32 s69, s68, 7
	s_bfe_u32 s7, s68, 0x20008
	s_lshl_b32 s81, s0, 8
	s_mul_i32 s6, s80, 0x1e00000
	v_readlane_b32 s10, v255, 31
	s_mul_hi_u32 s1, s80, 0x1e00000
	v_readlane_b32 s11, v255, 32
	s_add_u32 s92, s10, s6
	s_addc_u32 s93, s11, s1
	s_or_b32 s6, s81, s69
	s_lshl_b32 s11, s80, 2
	s_or_b32 s10, s11, s7
	v_or_b32_e32 v2, s6, v151
	s_or_b32 s8, s6, 8
	s_add_i32 s10, s10, 8
	s_lshl_b32 s15, s0, 3
	v_lshl_add_u64 v[102:103], s[92:93], 0, v[154:155]
	v_mul_u32_u24_e32 v2, 0xf00, v2
	s_lshl_b32 s64, s7, 6
	s_lshl_b32 s18, s10, 13
	s_lshl_b32 s1, s80, 8
	s_add_i32 s28, s15, -2
	s_waitcnt vmcnt(22)
	v_lshl_add_u64 v[4:5], v[102:103], 0, v[2:3]
	v_or_b32_e32 v2, s8, v151
	s_lshl_b64 s[30:31], s[18:19], 6
	s_or_b32 s18, s1, s64
	s_mov_b32 s65, s19
	v_mul_u32_u24_e32 v2, 0xf00, v2
	s_max_i32 s1, s28, 0
	s_lshl_b64 s[60:61], s[18:19], 14
	v_lshl_add_u64 v[4:5], v[4:5], 0, s[64:65]
	v_lshl_add_u64 v[6:7], v[102:103], 0, v[2:3]
	v_lshl_add_u64 v[104:105], v[156:157], 0, s[30:31]
	v_lshl_or_b32 v2, s1, 11, v160
	v_lshl_add_u64 v[6:7], v[6:7], 0, s[64:65]
	global_load_dwordx4 v[38:41], v[4:5], off offset:1536 nt
	global_load_dwordx4 v[42:45], v[6:7], off offset:1536 nt
	s_waitcnt vmcnt(21)
	v_lshl_add_u64 v[106:107], v[164:165], 0, s[60:61]
	v_lshl_add_u64 v[4:5], v[104:105], 0, v[2:3]
	s_lshl_b32 s18, s1, 12
	global_load_dwordx4 v[90:93], v[4:5], off
	global_load_dwordx4 v[86:89], v[4:5], off offset:1024
	v_lshl_add_u64 v[4:5], v[106:107], 0, s[18:19]
	global_load_dwordx4 v[82:85], v[4:5], off
	global_load_dwordx4 v[78:81], v[4:5], off offset:1024
	global_load_dwordx4 v[74:77], v[4:5], off offset:2048
	global_load_dwordx4 v[70:73], v[4:5], off offset:3072
	s_mul_i32 s1, s7, 0xa04
	s_lshl_b32 s29, s69, 2
	v_mov_b32_e32 v4, v3
	v_mov_b32_e32 v5, v3
	s_sub_i32 s29, s1, s29
	v_mov_b32_e32 v2, v3
	v_mov_b64_e32 v[8:9], v[4:5]
	s_waitcnt vmcnt(28)
	v_mov_b64_e32 v[12:13], v[4:5]
	v_mov_b64_e32 v[16:17], v[4:5]
	s_waitcnt vmcnt(26)
	v_mov_b64_e32 v[20:21], v[4:5]
	v_mov_b64_e32 v[24:25], v[4:5]
	s_waitcnt vmcnt(24)
	v_mov_b64_e32 v[28:29], v[4:5]
	v_mov_b64_e32 v[32:33], v[4:5]
	s_waitcnt vmcnt(22)
	v_mov_b64_e32 v[36:37], v[4:5]
	s_mov_b32 s18, -2
	v_add_u32_e32 v108, s29, v181
	v_mov_b32_e32 v114, 0xf149f2ca
	v_mov_b32_e32 v115, 0
	v_mov_b64_e32 v[6:7], v[2:3]
	v_mov_b64_e32 v[10:11], v[2:3]
	v_mov_b64_e32 v[14:15], v[2:3]
	v_mov_b64_e32 v[18:19], v[2:3]
	v_mov_b64_e32 v[22:23], v[2:3]
	v_mov_b64_e32 v[26:27], v[2:3]
	v_mov_b64_e32 v[30:31], v[2:3]
	v_mov_b64_e32 v[34:35], v[2:3]
	v_mov_b32_e32 v113, 0
	v_mov_b32_e32 v112, 0xf149f2ca
	s_add_i32 s29, s18, 3
	s_min_i32 s29, s29, 11
	s_add_i32 s29, s29, s28
	s_waitcnt vmcnt(18)
	v_med3_i32 v54, s29, 0, v184
	v_lshl_or_b32 v2, v54, 11, v160
	v_lshl_add_u64 v[4:5], v[104:105], 0, v[2:3]
	v_lshlrev_b32_e32 v2, 12, v54
	global_load_dwordx4 v[46:49], v[4:5], off
	global_load_dwordx4 v[50:53], v[4:5], off offset:1024
	v_lshl_add_u64 v[4:5], v[106:107], 0, v[2:3]
	global_load_dwordx4 v[54:57], v[4:5], off
	global_load_dwordx4 v[58:61], v[4:5], off offset:1024
	global_load_dwordx4 v[62:65], v[4:5], off offset:2048
	global_load_dwordx4 v[66:69], v[4:5], off offset:3072
.LBB0_749:
	s_add_i32 s29, s18, 4
	s_min_i32 s29, s29, 11
	s_add_i32 s29, s29, s28
	s_waitcnt vmcnt(24)
	v_med3_i32 v216, s29, 0, v184
	v_lshl_or_b32 v2, v216, 11, v160
	v_lshl_add_u64 v[4:5], v[104:105], 0, v[2:3]
	v_lshlrev_b32_e32 v2, 12, v216
	global_load_dwordx4 v[208:211], v[4:5], off
	global_load_dwordx4 v[212:215], v[4:5], off offset:1024
	v_lshl_add_u64 v[4:5], v[106:107], 0, v[2:3]
	global_load_dwordx4 v[216:219], v[4:5], off
	global_load_dwordx4 v[220:223], v[4:5], off offset:1024
	global_load_dwordx4 v[224:227], v[4:5], off offset:2048
	global_load_dwordx4 v[228:231], v[4:5], off offset:3072
	s_add_i32 s29, s15, s18
	s_cmpk_gt_u32 s29, 0xff
	s_cbranch_scc1 .Lpf2e_755
	s_waitcnt vmcnt(20)
	ds_read2_b32 v[94:95], v108 offset0:8 offset1:9
	ds_read2_b32 v[96:97], v108 offset0:10 offset1:11
	ds_read2_b32 v[116:117], v108 offset0:24 offset1:25
	ds_read2_b32 v[118:119], v108 offset0:26 offset1:27
	s_waitcnt vmcnt(17) lgkmcnt(2)
	v_mfma_f32_16x16x32_fp8_fp8 v[94:97], v[90:91], v[38:39], v[94:97]
	v_mfma_f32_16x16x32_fp8_fp8 v[98:101], v[92:93], v[40:41], v[94:97]
	s_waitcnt vmcnt(16) lgkmcnt(0)
	v_mfma_f32_16x16x32_fp8_fp8 v[94:97], v[86:87], v[38:39], v[116:119]
	v_mfma_f32_16x16x32_fp8_fp8 v[94:97], v[88:89], v[40:41], v[94:97]
	s_nop 4
	v_max3_f32 v2, v98, v99, v100
	s_nop 1
	v_max3_f32 v5, v101, v94, v95
	v_max3_f32 v2, v2, v96, v97
	v_max_f32_e32 v2, v2, v5
	v_mov_b32_e32 v4, v2
	s_nop 1
	v_permlane16_swap_b32_e32 v2, v4
	v_max_f32_e32 v2, v2, v4
	v_mov_b32_e32 v4, v2
	s_nop 1
	v_permlane32_swap_b32_e32 v2, v4
	v_max_f32_e32 v2, v2, v4
	v_cmp_gt_f32_e32 vcc, v2, v112
	s_cbranch_vccz .Lpf2e_752
	v_max_f32_e32 v2, v2, v2
	v_max_f32_e32 v4, v112, v112
	v_max_f32_e32 v4, v4, v2
	v_sub_f32_e32 v2, v112, v4
	v_exp_f32_e32 v2, v2
	v_mov_b32_e32 v112, v4
	v_mul_f32_e32 v113, v113, v2
	v_pk_mul_f32 v[36:37], v[36:37], v[2:3] op_sel_hi:[1,0]
	v_pk_mul_f32 v[34:35], v[34:35], v[2:3] op_sel_hi:[1,0]
	v_pk_mul_f32 v[32:33], v[32:33], v[2:3] op_sel_hi:[1,0]
	v_pk_mul_f32 v[30:31], v[30:31], v[2:3] op_sel_hi:[1,0]
	v_pk_mul_f32 v[28:29], v[28:29], v[2:3] op_sel_hi:[1,0]
	v_pk_mul_f32 v[26:27], v[26:27], v[2:3] op_sel_hi:[1,0]
	v_pk_mul_f32 v[24:25], v[24:25], v[2:3] op_sel_hi:[1,0]
	v_pk_mul_f32 v[22:23], v[22:23], v[2:3] op_sel_hi:[1,0]
.Lpf2e_752:
	v_sub_f32_e32 v2, v98, v112
	v_sub_f32_e32 v4, v99, v112
	v_sub_f32_e32 v5, v100, v112
	v_sub_f32_e32 v98, v101, v112
	v_sub_f32_e32 v94, v94, v112
	v_sub_f32_e32 v95, v95, v112
	v_sub_f32_e32 v96, v96, v112
	v_sub_f32_e32 v97, v97, v112
	v_exp_f32_e32 v2, v2
	v_exp_f32_e32 v4, v4
	v_exp_f32_e32 v5, v5
	v_exp_f32_e32 v98, v98
	v_exp_f32_e32 v94, v94
	v_exp_f32_e32 v95, v95
	v_exp_f32_e32 v96, v96
	v_exp_f32_e32 v97, v97
	v_cvt_pk_bf16_f32 v116, v2, v4
	v_cvt_pk_bf16_f32 v117, v5, v98
	v_cvt_pk_bf16_f32 v118, v94, v95
	v_cvt_pk_bf16_f32 v119, v96, v97
	s_waitcnt vmcnt(15)
	s_nop 0
	v_mfma_f32_16x16x32_bf16 v[34:37], v[82:85], v[116:119], v[34:37]
	s_waitcnt vmcnt(14)
	v_mfma_f32_16x16x32_bf16 v[30:33], v[78:81], v[116:119], v[30:33]
	s_waitcnt vmcnt(13)
	v_mfma_f32_16x16x32_bf16 v[26:29], v[74:77], v[116:119], v[26:29]
	s_waitcnt vmcnt(12)
	v_mfma_f32_16x16x32_bf16 v[22:25], v[70:73], v[116:119], v[22:25]
	ds_read2_b32 v[116:117], v108 offset1:1
	ds_read2_b32 v[118:119], v108 offset0:2 offset1:3
	ds_read2_b32 v[120:121], v108 offset0:16 offset1:17
	ds_read2_b32 v[122:123], v108 offset0:18 offset1:19
	s_waitcnt lgkmcnt(2)
	v_mfma_f32_16x16x32_fp8_fp8 v[116:119], v[90:91], v[42:43], v[116:119]
	v_mfma_f32_16x16x32_fp8_fp8 v[90:93], v[92:93], v[44:45], v[116:119]
	s_waitcnt lgkmcnt(0)
	v_mfma_f32_16x16x32_fp8_fp8 v[116:119], v[86:87], v[42:43], v[120:123]
	v_mfma_f32_16x16x32_fp8_fp8 v[86:89], v[88:89], v[44:45], v[116:119]
	v_add_f32_e32 v2, v4, v2
	v_add_f32_e32 v2, v5, v2
	v_add_f32_e32 v2, v98, v2
	v_add_f32_e32 v2, v94, v2
	v_add_f32_e32 v2, v95, v2
	v_add_f32_e32 v2, v96, v2
	v_add_f32_e32 v2, v97, v2
	v_add_f32_e32 v113, v113, v2
	v_max3_f32 v99, v90, v91, v92
	v_max3_f32 v101, v93, v86, v87
	v_max3_f32 v99, v99, v88, v89
	v_max_f32_e32 v99, v99, v101
	v_mov_b32_e32 v100, v99
	s_nop 1
	v_permlane16_swap_b32_e32 v99, v100
	v_max_f32_e32 v99, v99, v100
	v_mov_b32_e32 v100, v99
	s_nop 1
	v_permlane32_swap_b32_e32 v99, v100
	v_max_f32_e32 v99, v99, v100
	v_cmp_gt_f32_e32 vcc, v99, v114
	s_cbranch_vccz .Lpf2e_754
	v_max_f32_e32 v99, v99, v99
	v_max_f32_e32 v100, v114, v114
	v_max_f32_e32 v99, v100, v99
	v_sub_f32_e32 v100, v114, v99
	v_exp_f32_e32 v100, v100
	v_mov_b32_e32 v114, v99
	v_mul_f32_e32 v115, v115, v100
	v_pk_mul_f32 v[20:21], v[20:21], v[100:101] op_sel_hi:[1,0]
	v_pk_mul_f32 v[18:19], v[18:19], v[100:101] op_sel_hi:[1,0]
	v_pk_mul_f32 v[16:17], v[16:17], v[100:101] op_sel_hi:[1,0]
	v_pk_mul_f32 v[14:15], v[14:15], v[100:101] op_sel_hi:[1,0]
	v_pk_mul_f32 v[12:13], v[12:13], v[100:101] op_sel_hi:[1,0]
	v_pk_mul_f32 v[10:11], v[10:11], v[100:101] op_sel_hi:[1,0]
	v_pk_mul_f32 v[8:9], v[8:9], v[100:101] op_sel_hi:[1,0]
	v_pk_mul_f32 v[6:7], v[6:7], v[100:101] op_sel_hi:[1,0]

.Lpf2e_755:
	s_add_i32 s18, s18, 1
	s_cmp_lg_u32 s18, 10
	v_add_u32_e32 v108, 0x80, v108
	s_waitcnt vmcnt(6)
	v_mov_b64_e32 v[72:73], v[68:69]
	v_mov_b64_e32 v[76:77], v[64:65]
	v_mov_b64_e32 v[80:81], v[60:61]
	v_mov_b64_e32 v[84:85], v[56:57]
	v_mov_b64_e32 v[92:93], v[48:49]
	v_mov_b64_e32 v[88:89], v[52:53]
	v_mov_b64_e32 v[70:71], v[66:67]
	v_mov_b64_e32 v[74:75], v[62:63]
	v_mov_b64_e32 v[78:79], v[58:59]
	v_mov_b64_e32 v[82:83], v[54:55]
	v_mov_b64_e32 v[90:91], v[46:47]
	v_mov_b64_e32 v[86:87], v[50:51]
.Lpf2_749_odd:
	s_add_i32 s29, s18, 4
	s_min_i32 s29, s29, 11
	s_add_i32 s29, s29, s28
	s_waitcnt vmcnt(24)
	v_med3_i32 v54, s29, 0, v184
	v_lshl_or_b32 v2, v54, 11, v160
	v_lshl_add_u64 v[4:5], v[104:105], 0, v[2:3]
	v_lshlrev_b32_e32 v2, 12, v54
	global_load_dwordx4 v[46:49], v[4:5], off
	global_load_dwordx4 v[50:53], v[4:5], off offset:1024
	v_lshl_add_u64 v[4:5], v[106:107], 0, v[2:3]
	global_load_dwordx4 v[54:57], v[4:5], off
	global_load_dwordx4 v[58:61], v[4:5], off offset:1024
	global_load_dwordx4 v[62:65], v[4:5], off offset:2048
	global_load_dwordx4 v[66:69], v[4:5], off offset:3072
	s_add_i32 s29, s15, s18
	s_cmpk_gt_u32 s29, 0xff
	s_cbranch_scc1 .LBB0_755
	s_waitcnt vmcnt(20)
	ds_read2_b32 v[94:95], v108 offset0:8 offset1:9
	ds_read2_b32 v[96:97], v108 offset0:10 offset1:11
	ds_read2_b32 v[116:117], v108 offset0:24 offset1:25
	ds_read2_b32 v[118:119], v108 offset0:26 offset1:27
	s_waitcnt vmcnt(17) lgkmcnt(2)
	v_mfma_f32_16x16x32_fp8_fp8 v[94:97], v[90:91], v[38:39], v[94:97]
	v_mfma_f32_16x16x32_fp8_fp8 v[98:101], v[92:93], v[40:41], v[94:97]
	s_waitcnt vmcnt(16) lgkmcnt(0)
	v_mfma_f32_16x16x32_fp8_fp8 v[94:97], v[86:87], v[38:39], v[116:119]
	v_mfma_f32_16x16x32_fp8_fp8 v[94:97], v[88:89], v[40:41], v[94:97]
	s_nop 4
	v_max3_f32 v2, v98, v99, v100
	s_nop 1
	v_max3_f32 v5, v101, v94, v95
	v_max3_f32 v2, v2, v96, v97
	v_max_f32_e32 v2, v2, v5
	v_mov_b32_e32 v4, v2
	s_nop 1
	v_permlane16_swap_b32_e32 v2, v4
	v_max_f32_e32 v2, v2, v4
	v_mov_b32_e32 v4, v2
	s_nop 1
	v_permlane32_swap_b32_e32 v2, v4
	v_max_f32_e32 v2, v2, v4
	v_cmp_gt_f32_e32 vcc, v2, v112
	s_cbranch_vccz .LBB0_752
	v_max_f32_e32 v2, v2, v2
	v_max_f32_e32 v4, v112, v112
	v_max_f32_e32 v4, v4, v2
	v_sub_f32_e32 v2, v112, v4
	v_exp_f32_e32 v2, v2
	v_mov_b32_e32 v112, v4
	v_mul_f32_e32 v113, v113, v2
	v_pk_mul_f32 v[36:37], v[36:37], v[2:3] op_sel_hi:[1,0]
	v_pk_mul_f32 v[34:35], v[34:35], v[2:3] op_sel_hi:[1,0]
	v_pk_mul_f32 v[32:33], v[32:33], v[2:3] op_sel_hi:[1,0]
	v_pk_mul_f32 v[30:31], v[30:31], v[2:3] op_sel_hi:[1,0]
	v_pk_mul_f32 v[28:29], v[28:29], v[2:3] op_sel_hi:[1,0]
	v_pk_mul_f32 v[26:27], v[26:27], v[2:3] op_sel_hi:[1,0]
	v_pk_mul_f32 v[24:25], v[24:25], v[2:3] op_sel_hi:[1,0]
	v_pk_mul_f32 v[22:23], v[22:23], v[2:3] op_sel_hi:[1,0]

.LBB0_755:
	s_add_i32 s18, s18, 1
	s_cmp_lg_u32 s18, 10
	v_add_u32_e32 v108, 0x80, v108
	s_cbranch_scc0 .Lpf2_749_exit
	s_waitcnt vmcnt(6)
	v_mov_b64_e32 v[72:73], v[230:231]
	v_mov_b64_e32 v[76:77], v[226:227]
	v_mov_b64_e32 v[80:81], v[222:223]
	v_mov_b64_e32 v[84:85], v[218:219]
	v_mov_b64_e32 v[92:93], v[210:211]
	v_mov_b64_e32 v[88:89], v[214:215]
	v_mov_b64_e32 v[70:71], v[228:229]
	v_mov_b64_e32 v[74:75], v[224:225]
	v_mov_b64_e32 v[78:79], v[220:221]
	v_mov_b64_e32 v[82:83], v[216:217]
	v_mov_b64_e32 v[90:91], v[208:209]
	v_mov_b64_e32 v[86:87], v[212:213]
	s_branch .LBB0_749
.Lpf2_749_exit:
	s_waitcnt vmcnt(6)
.LBB0_757:
	s_lshr_b32 s30, s8, 2
	s_add_i32 s8, s11, s7
	s_add_i32 s7, s8, 16
	s_lshl_b32 s18, s7, 13
	s_lshr_b32 s15, s6, 2
	s_lshl_b64 s[28:29], s[18:19], 6
	v_readlane_b32 s60, v255, 39
	v_readlane_b32 s61, v255, 40
	s_add_u32 s31, s60, s28
	s_addc_u32 s60, s61, s29
	s_lshl_b32 s18, s10, 6
	s_lshl_b64 s[10:11], s[18:19], 14
	v_readlane_b32 s28, v255, 60
	v_readlane_b32 s29, v255, 61
	s_add_u32 s18, s28, s10
	s_addc_u32 s61, s29, s11
	s_and_b32 s62, s68, 3
	v_or_b32_e32 v2, s15, v159
	v_lshl_or_b32 v2, v2, 2, s62
	s_movk_i32 s15, 0xf00
	v_mad_u64_u32 v[4:5], s[28:29], v2, s15, v[102:103]
	v_or_b32_e32 v2, s30, v159
	s_lshl_b32 s10, s0, 1
	v_lshl_or_b32 v2, v2, 2, s62
	s_add_i32 s11, s10, -2
	s_waitcnt vmcnt(13)
	v_mad_u64_u32 v[38:39], s[28:29], v2, s15, v[102:103]
	s_lshl_b32 s15, s62, 17
	s_add_u32 s28, s31, s15
	s_addc_u32 s29, s60, 0
	s_lshl_b32 s15, s62, 18
	v_lshl_add_u64 v[4:5], v[4:5], 0, s[64:65]
	s_waitcnt vmcnt(12)
	v_lshl_add_u64 v[42:43], v[38:39], 0, s[64:65]
	v_lshl_add_u64 v[104:105], s[28:29], 0, v[154:155]
	s_add_u32 s28, s18, s15
	global_load_dwordx4 v[38:41], v[4:5], off offset:1792 nt
	s_nop 0
	global_load_dwordx4 v[42:45], v[42:43], off offset:1792 nt
	s_addc_u32 s29, s61, 0
	v_lshlrev_b32_e32 v4, 1, v158
	v_mov_b32_e32 v5, v3
	s_waitcnt vmcnt(7)
	v_lshl_add_u64 v[46:47], s[28:29], 0, v[4:5]
	v_med3_i32 v5, s11, 0, 63
	v_lshlrev_b32_e32 v102, 1, v162
	v_mov_b32_e32 v103, v3
	v_lshl_or_b32 v2, v5, 11, v160
	v_lshl_add_u64 v[106:107], v[46:47], 0, v[102:103]
	v_lshl_add_u64 v[46:47], v[104:105], 0, v[2:3]
	v_lshlrev_b32_e32 v2, 12, v5
	global_load_dwordx4 v[90:93], v[46:47], off
	global_load_dwordx4 v[86:89], v[46:47], off offset:1024
	v_lshl_add_u64 v[46:47], v[106:107], 0, v[2:3]
	global_load_dwordx4 v[82:85], v[46:47], off
	global_load_dwordx4 v[78:81], v[46:47], off offset:1024
	global_load_dwordx4 v[74:77], v[46:47], off offset:2048
	global_load_dwordx4 v[70:73], v[46:47], off offset:3072
	s_add_i32 s18, s1, s81
	s_and_b32 s6, s6, 0x1ffc
	s_sub_i32 s6, s18, s6
	v_add_u32_e32 v5, s6, v182
	s_add_i32 s6, s81, s69
	s_add_i32 s6, s6, 8
	s_and_b32 s6, s6, 0x7ffc
	s_sub_i32 s6, s18, s6
	s_mov_b32 s15, 1
	v_add_u32_e32 v103, s6, v182
	s_min_i32 s6, s15, 5
	s_add_i32 s6, s6, s11
	s_waitcnt vmcnt(11)
	v_med3_i32 v54, s6, 0, 63
	v_lshl_or_b32 v2, v54, 11, v160
	v_lshl_add_u64 v[50:51], v[104:105], 0, v[2:3]
	v_lshlrev_b32_e32 v2, 12, v54
	s_waitcnt vmcnt(8)
	v_lshl_add_u64 v[66:67], v[106:107], 0, v[2:3]
	global_load_dwordx4 v[46:49], v[50:51], off
	s_nop 0
	global_load_dwordx4 v[50:53], v[50:51], off offset:1024
	s_nop 0
	global_load_dwordx4 v[54:57], v[66:67], off
	global_load_dwordx4 v[58:61], v[66:67], off offset:1024
	global_load_dwordx4 v[62:65], v[66:67], off offset:2048
	s_nop 0
	global_load_dwordx4 v[66:69], v[66:67], off offset:3072
.LBB0_758:
	s_add_i32 s6, s15, 1
	s_min_i32 s6, s6, 5
	s_add_i32 s6, s6, s11
	s_waitcnt vmcnt(17)
	v_med3_i32 v216, s6, 0, 63
	v_lshl_or_b32 v2, v216, 11, v160
	v_lshl_add_u64 v[212:213], v[104:105], 0, v[2:3]
	v_lshlrev_b32_e32 v2, 12, v216
	s_waitcnt vmcnt(14)
	v_lshl_add_u64 v[228:229], v[106:107], 0, v[2:3]
	global_load_dwordx4 v[208:211], v[212:213], off
	s_nop 0
	global_load_dwordx4 v[212:215], v[212:213], off offset:1024
	s_nop 0
	global_load_dwordx4 v[216:219], v[228:229], off
	global_load_dwordx4 v[220:223], v[228:229], off offset:1024
	global_load_dwordx4 v[224:227], v[228:229], off offset:2048
	s_nop 0
	global_load_dwordx4 v[228:231], v[228:229], off offset:3072
	s_add_i32 s6, s10, s15
	s_add_i32 s6, s6, -3
	s_cmp_gt_u32 s6, 63
	s_cbranch_scc1 .Lpf2e_764
	ds_read2_b32 v[94:95], v5 offset1:1
	ds_read2_b32 v[96:97], v5 offset0:2 offset1:3
	ds_read2_b32 v[108:109], v5 offset0:16 offset1:17
	ds_read2_b32 v[110:111], v5 offset0:18 offset1:19
	s_waitcnt vmcnt(17) lgkmcnt(2)
	v_mfma_f32_16x16x32_fp8_fp8 v[94:97], v[90:91], v[38:39], v[94:97]
	v_mfma_f32_16x16x32_fp8_fp8 v[98:101], v[92:93], v[40:41], v[94:97]
	s_waitcnt vmcnt(16) lgkmcnt(0)
	v_mfma_f32_16x16x32_fp8_fp8 v[94:97], v[86:87], v[38:39], v[108:111]
	v_mfma_f32_16x16x32_fp8_fp8 v[94:97], v[88:89], v[40:41], v[94:97]
	s_nop 4
	v_max3_f32 v2, v98, v99, v100
	s_nop 1
	v_max3_f32 v109, v101, v94, v95
	v_max3_f32 v2, v2, v96, v97
	v_max_f32_e32 v2, v2, v109
	v_mov_b32_e32 v108, v2
	s_nop 1
	v_permlane16_swap_b32_e32 v2, v108
	v_max_f32_e32 v2, v2, v108
	v_mov_b32_e32 v108, v2
	s_nop 1
	v_permlane32_swap_b32_e32 v2, v108
	v_max_f32_e32 v2, v2, v108
	v_cmp_gt_f32_e32 vcc, v2, v112
	s_cbranch_vccz .Lpf2e_761
	v_max_f32_e32 v2, v2, v2
	v_max_f32_e32 v108, v112, v112
	v_max_f32_e32 v108, v108, v2
	v_sub_f32_e32 v2, v112, v108
	v_exp_f32_e32 v2, v2
	v_mov_b32_e32 v112, v108
	v_mul_f32_e32 v113, v113, v2
	v_pk_mul_f32 v[36:37], v[36:37], v[2:3] op_sel_hi:[1,0]
	v_pk_mul_f32 v[34:35], v[34:35], v[2:3] op_sel_hi:[1,0]
	v_pk_mul_f32 v[32:33], v[32:33], v[2:3] op_sel_hi:[1,0]
	v_pk_mul_f32 v[30:31], v[30:31], v[2:3] op_sel_hi:[1,0]
	v_pk_mul_f32 v[28:29], v[28:29], v[2:3] op_sel_hi:[1,0]
	v_pk_mul_f32 v[26:27], v[26:27], v[2:3] op_sel_hi:[1,0]
	v_pk_mul_f32 v[24:25], v[24:25], v[2:3] op_sel_hi:[1,0]
	v_pk_mul_f32 v[22:23], v[22:23], v[2:3] op_sel_hi:[1,0]
.Lpf2e_761:
	v_sub_f32_e32 v2, v98, v112
	v_sub_f32_e32 v98, v99, v112
	v_sub_f32_e32 v99, v100, v112
	v_sub_f32_e32 v100, v101, v112
	v_sub_f32_e32 v94, v94, v112
	v_sub_f32_e32 v95, v95, v112
	v_sub_f32_e32 v96, v96, v112
	v_sub_f32_e32 v97, v97, v112
	v_exp_f32_e32 v2, v2
	v_exp_f32_e32 v98, v98
	v_exp_f32_e32 v99, v99
	v_exp_f32_e32 v100, v100
	v_exp_f32_e32 v94, v94
	v_exp_f32_e32 v95, v95
	v_exp_f32_e32 v96, v96
	v_exp_f32_e32 v97, v97
	v_cvt_pk_bf16_f32 v108, v2, v98
	v_cvt_pk_bf16_f32 v109, v99, v100
	v_cvt_pk_bf16_f32 v110, v94, v95
	v_cvt_pk_bf16_f32 v111, v96, v97
	s_waitcnt vmcnt(15)
	s_nop 0
	v_mfma_f32_16x16x32_bf16 v[34:37], v[82:85], v[108:111], v[34:37]
	s_waitcnt vmcnt(14)
	v_mfma_f32_16x16x32_bf16 v[30:33], v[78:81], v[108:111], v[30:33]
	s_waitcnt vmcnt(13)
	v_mfma_f32_16x16x32_bf16 v[26:29], v[74:77], v[108:111], v[26:29]
	s_waitcnt vmcnt(12)
	v_mfma_f32_16x16x32_bf16 v[22:25], v[70:73], v[108:111], v[22:25]
	ds_read2_b32 v[108:109], v103 offset1:1
	ds_read2_b32 v[110:111], v103 offset0:2 offset1:3
	ds_read2_b32 v[116:117], v103 offset0:16 offset1:17
	ds_read2_b32 v[118:119], v103 offset0:18 offset1:19
	s_waitcnt lgkmcnt(2)
	v_mfma_f32_16x16x32_fp8_fp8 v[108:111], v[90:91], v[42:43], v[108:111]
	v_mfma_f32_16x16x32_fp8_fp8 v[90:93], v[92:93], v[44:45], v[108:111]
	s_waitcnt lgkmcnt(0)
	v_mfma_f32_16x16x32_fp8_fp8 v[108:111], v[86:87], v[42:43], v[116:119]
	v_mfma_f32_16x16x32_fp8_fp8 v[86:89], v[88:89], v[44:45], v[108:111]
	v_add_f32_e32 v2, v98, v2
	v_add_f32_e32 v2, v99, v2
	v_add_f32_e32 v2, v100, v2
	v_add_f32_e32 v2, v94, v2
	v_add_f32_e32 v2, v95, v2
	v_add_f32_e32 v2, v96, v2
	v_add_f32_e32 v2, v97, v2
	v_add_f32_e32 v113, v113, v2
	v_max3_f32 v101, v90, v91, v92
	v_max3_f32 v109, v93, v86, v87
	v_max3_f32 v101, v101, v88, v89
	v_max_f32_e32 v101, v101, v109
	v_mov_b32_e32 v108, v101
	s_nop 1
	v_permlane16_swap_b32_e32 v101, v108
	v_max_f32_e32 v101, v101, v108
	v_mov_b32_e32 v108, v101
	s_nop 1
	v_permlane32_swap_b32_e32 v101, v108
	v_max_f32_e32 v101, v101, v108
	v_cmp_gt_f32_e32 vcc, v101, v114
	s_cbranch_vccz .Lpf2e_763
	v_max_f32_e32 v101, v101, v101
	v_max_f32_e32 v108, v114, v114
	v_max_f32_e32 v101, v108, v101
	v_sub_f32_e32 v108, v114, v101
	v_exp_f32_e32 v108, v108
	v_mov_b32_e32 v114, v101
	v_mul_f32_e32 v115, v115, v108
	v_pk_mul_f32 v[20:21], v[20:21], v[108:109] op_sel_hi:[1,0]
	v_pk_mul_f32 v[18:19], v[18:19], v[108:109] op_sel_hi:[1,0]
	v_pk_mul_f32 v[16:17], v[16:17], v[108:109] op_sel_hi:[1,0]
	v_pk_mul_f32 v[14:15], v[14:15], v[108:109] op_sel_hi:[1,0]
	v_pk_mul_f32 v[12:13], v[12:13], v[108:109] op_sel_hi:[1,0]
	v_pk_mul_f32 v[10:11], v[10:11], v[108:109] op_sel_hi:[1,0]
	v_pk_mul_f32 v[8:9], v[8:9], v[108:109] op_sel_hi:[1,0]
	v_pk_mul_f32 v[6:7], v[6:7], v[108:109] op_sel_hi:[1,0]

.Lpf2e_764:
	s_add_i32 s15, s15, 1
	v_add_u32_e32 v5, 0x80, v5
	s_cmp_lg_u32 s15, 7
	v_add_u32_e32 v103, 0x80, v103
	s_waitcnt vmcnt(6)
	v_mov_b64_e32 v[72:73], v[68:69]
	v_mov_b64_e32 v[76:77], v[64:65]
	v_mov_b64_e32 v[80:81], v[60:61]
	v_mov_b64_e32 v[84:85], v[56:57]
	v_mov_b64_e32 v[92:93], v[48:49]
	v_mov_b64_e32 v[88:89], v[52:53]
	v_mov_b64_e32 v[70:71], v[66:67]
	v_mov_b64_e32 v[74:75], v[62:63]
	v_mov_b64_e32 v[78:79], v[58:59]
	v_mov_b64_e32 v[82:83], v[54:55]
	v_mov_b64_e32 v[90:91], v[46:47]
	v_mov_b64_e32 v[86:87], v[50:51]
.Lpf2_758_odd:
	s_add_i32 s6, s15, 1
	s_min_i32 s6, s6, 5
	s_add_i32 s6, s6, s11
	s_waitcnt vmcnt(17)
	v_med3_i32 v54, s6, 0, 63
	v_lshl_or_b32 v2, v54, 11, v160
	v_lshl_add_u64 v[50:51], v[104:105], 0, v[2:3]
	v_lshlrev_b32_e32 v2, 12, v54
	s_waitcnt vmcnt(14)
	v_lshl_add_u64 v[66:67], v[106:107], 0, v[2:3]
	global_load_dwordx4 v[46:49], v[50:51], off
	s_nop 0
	global_load_dwordx4 v[50:53], v[50:51], off offset:1024
	s_nop 0
	global_load_dwordx4 v[54:57], v[66:67], off
	global_load_dwordx4 v[58:61], v[66:67], off offset:1024
	global_load_dwordx4 v[62:65], v[66:67], off offset:2048
	s_nop 0
	global_load_dwordx4 v[66:69], v[66:67], off offset:3072
	s_add_i32 s6, s10, s15
	s_add_i32 s6, s6, -3
	s_cmp_gt_u32 s6, 63
	s_cbranch_scc1 .LBB0_764
	ds_read2_b32 v[94:95], v5 offset1:1
	ds_read2_b32 v[96:97], v5 offset0:2 offset1:3
	ds_read2_b32 v[108:109], v5 offset0:16 offset1:17
	ds_read2_b32 v[110:111], v5 offset0:18 offset1:19
	s_waitcnt vmcnt(17) lgkmcnt(2)
	v_mfma_f32_16x16x32_fp8_fp8 v[94:97], v[90:91], v[38:39], v[94:97]
	v_mfma_f32_16x16x32_fp8_fp8 v[98:101], v[92:93], v[40:41], v[94:97]
	s_waitcnt vmcnt(16) lgkmcnt(0)
	v_mfma_f32_16x16x32_fp8_fp8 v[94:97], v[86:87], v[38:39], v[108:111]
	v_mfma_f32_16x16x32_fp8_fp8 v[94:97], v[88:89], v[40:41], v[94:97]
	s_nop 4
	v_max3_f32 v2, v98, v99, v100
	s_nop 1
	v_max3_f32 v109, v101, v94, v95
	v_max3_f32 v2, v2, v96, v97
	v_max_f32_e32 v2, v2, v109
	v_mov_b32_e32 v108, v2
	s_nop 1
	v_permlane16_swap_b32_e32 v2, v108
	v_max_f32_e32 v2, v2, v108
	v_mov_b32_e32 v108, v2
	s_nop 1
	v_permlane32_swap_b32_e32 v2, v108
	v_max_f32_e32 v2, v2, v108
	v_cmp_gt_f32_e32 vcc, v2, v112
	s_cbranch_vccz .LBB0_761
	v_max_f32_e32 v2, v2, v2
	v_max_f32_e32 v108, v112, v112
	v_max_f32_e32 v108, v108, v2
	v_sub_f32_e32 v2, v112, v108
	v_exp_f32_e32 v2, v2
	v_mov_b32_e32 v112, v108
	v_mul_f32_e32 v113, v113, v2
	v_pk_mul_f32 v[36:37], v[36:37], v[2:3] op_sel_hi:[1,0]
	v_pk_mul_f32 v[34:35], v[34:35], v[2:3] op_sel_hi:[1,0]
	v_pk_mul_f32 v[32:33], v[32:33], v[2:3] op_sel_hi:[1,0]
	v_pk_mul_f32 v[30:31], v[30:31], v[2:3] op_sel_hi:[1,0]
	v_pk_mul_f32 v[28:29], v[28:29], v[2:3] op_sel_hi:[1,0]
	v_pk_mul_f32 v[26:27], v[26:27], v[2:3] op_sel_hi:[1,0]
	v_pk_mul_f32 v[24:25], v[24:25], v[2:3] op_sel_hi:[1,0]
	v_pk_mul_f32 v[22:23], v[22:23], v[2:3] op_sel_hi:[1,0]

.LBB0_764:
	s_add_i32 s15, s15, 1
	v_add_u32_e32 v5, 0x80, v5
	s_cmp_lg_u32 s15, 7
	v_add_u32_e32 v103, 0x80, v103
	s_cbranch_scc0 .Lpf2_758_exit
	s_waitcnt vmcnt(6)
	v_mov_b64_e32 v[72:73], v[230:231]
	v_mov_b64_e32 v[76:77], v[226:227]
	v_mov_b64_e32 v[80:81], v[222:223]
	v_mov_b64_e32 v[84:85], v[218:219]
	v_mov_b64_e32 v[92:93], v[210:211]
	v_mov_b64_e32 v[88:89], v[214:215]
	v_mov_b64_e32 v[70:71], v[228:229]
	v_mov_b64_e32 v[74:75], v[224:225]
	v_mov_b64_e32 v[78:79], v[220:221]
	v_mov_b64_e32 v[82:83], v[216:217]
	v_mov_b64_e32 v[90:91], v[208:209]
	v_mov_b64_e32 v[86:87], v[212:213]
	s_branch .LBB0_758
